# window/SWA/sel distance-table builds de-looped (b128 fills + batched near lookups, 2 waves per head)
# speedup vs baseline: 1.0091x; 1.0016x over previous
.LBB0_1003:
	s_lshl_b32 s36, s37, 6
	s_lshl_b32 s12, s8, 8
	s_add_i32 s38, s36, s28
	s_lshl_b32 s6, s8, 6
	s_ashr_i32 s9, s8, 31
	s_ashr_i32 s13, s12, 31
	s_ashr_i32 s7, s6, 31
	s_lshl_b64 s[10:11], s[8:9], 21
	v_or_b32_e32 v130, s38, v134
	s_lshl_b64 s[12:13], s[12:13], 1
	s_add_u32 s12, s80, s12
	v_ashrrev_i32_e32 v131, 31, v130
	s_addc_u32 s13, s81, s13
	v_lshlrev_b64 v[2:3], 13, v[130:131]
	v_lshl_add_u64 v[2:3], s[12:13], 0, v[2:3]
	v_lshl_add_u64 v[2:3], v[2:3], 0, v[0:1]
	v_mov_b32_e32 v127, v1
	v_lshl_add_u64 v[2:3], v[2:3], 0, v[126:127]
	s_mov_b64 s[14:15], 0x1a00
	v_lshl_add_u64 v[4:5], v[2:3], 0, s[14:15]
	v_add_co_u32_e32 v2, vcc, s97, v2
	v_or_b32_e32 v128, 4, v130
	s_nop 0
	v_addc_co_u32_e32 v3, vcc, 0, v3, vcc
	v_ashrrev_i32_e32 v129, 31, v128
	global_load_dwordx4 v[42:45], v[2:3], off offset:2560
	global_load_dwordx4 v[46:49], v[4:5], off offset:64
	v_lshlrev_b64 v[2:3], 13, v[128:129]
	v_lshl_add_u64 v[2:3], s[12:13], 0, v[2:3]
	v_lshl_add_u64 v[2:3], v[2:3], 0, v[0:1]
	v_lshl_add_u64 v[2:3], v[2:3], 0, v[126:127]
	v_lshl_add_u64 v[6:7], v[2:3], 0, s[14:15]
	v_add_co_u32_e32 v2, vcc, s97, v2
	v_mov_b32_e32 v10, s64
	s_nop 0
	v_addc_co_u32_e32 v3, vcc, 0, v3, vcc
	global_load_dwordx4 v[2:5], v[2:3], off offset:2560
	s_nop 0
	global_load_dwordx4 v[6:9], v[6:7], off offset:64
	ds_read_b32 v10, v10
	s_lshl_b64 s[6:7], s[6:7], 1
	s_add_u32 s6, s92, s6
	s_addc_u32 s7, s93, s7
	s_lshl_b32 s22, s8, 2
	v_mov_b32_e32 v11, s65
	s_waitcnt lgkmcnt(0)
	v_readfirstlane_b32 s9, v10
	s_add_u32 s8, s82, s10
	ds_read_b32 v11, v11
	v_mov_b32_e32 v10, s9
	s_addc_u32 s9, s83, s11
	s_add_u32 s8, s8, 0x800000
	s_addc_u32 s9, s9, 0
	s_add_i32 s39, s36, 0xffffff80
	s_max_i32 s42, s39, 0
	s_lshl_b64 s[10:11], s[42:43], 13
	s_waitcnt lgkmcnt(0)
	v_readfirstlane_b32 s12, v11
	s_add_u32 s10, s6, s10
	v_add_u32_e32 v12, s22, v135
	v_mov_b32_e32 v11, s12
	s_addc_u32 s11, s7, s11
	s_lshl_b32 s12, s42, 1
	v_ashrrev_i32_e32 v13, 31, v12
	s_add_u32 s12, s8, s12
	v_lshl_add_u64 v[10:11], v[12:13], 2, v[10:11]
	s_addc_u32 s13, s9, 0
	flat_load_dword v127, v[10:11]
	v_lshl_add_u64 v[10:11], v[122:123], 1, s[10:11]
	v_lshl_add_u64 v[12:13], v[124:125], 1, s[12:13]
	s_waitcnt lgkmcnt(0)
	s_barrier
	global_load_dwordx4 v[14:17], v[10:11], off
	s_nop 0
	global_load_dwordx4 v[10:13], v[12:13], off
	s_sub_i32 s10, s36, 64
	s_max_i32 s42, s10, 0
	s_lshl_b64 s[10:11], s[42:43], 13
	s_lshl_b32 s42, s42, 1
	v_lshl_add_u64 v[18:19], v[122:123], 1, s[6:7]
	v_lshl_add_u64 v[20:21], v[124:125], 1, s[8:9]
	v_lshl_add_u64 v[22:23], v[18:19], 0, s[10:11]
	v_lshl_add_u64 v[24:25], v[20:21], 0, s[42:43]
	global_load_dwordx4 v[200:203], v[22:23], off
	global_load_dwordx4 v[204:207], v[24:25], off
	s_max_i32 s42, s36, 0
	s_lshl_b64 s[10:11], s[42:43], 13
	s_lshl_b32 s42, s42, 1
	v_lshl_add_u64 v[22:23], v[18:19], 0, s[10:11]
	v_lshl_add_u64 v[24:25], v[20:21], 0, s[42:43]
	global_load_dwordx4 v[208:211], v[22:23], off
	global_load_dwordx4 v[212:215], v[24:25], off
	s_and_saveexec_b64 s[10:11], s[0:1]
	s_cbranch_execz .LBB0_1010
	v_readfirstlane_b32 s12, v178
	s_lshr_b32 s12, s12, 7
	v_and_b32_e32 v88, 0x7f, v178
	s_mul_i32 s13, s12, 0x1220
	s_add_i32 s13, s13, 0x20000
	s_add_i32 s42, s22, s12
	s_lshl_b32 s42, s42, 2
	s_add_i32 s42, s42, 0x25520
	s_add_i32 s14, s13, 0xe00
	s_add_i32 s15, s13, 0x1000
	v_mov_b32_e32 v104, v88
	v_sub_u32_e32 v90, 0x7f, v104
	v_cvt_f32_u32_e32 v91, v90
	v_log_f32_e32 v91, v91
	v_cmp_gt_u32_e32 vcc, 16, v90
	v_mul_f32_e32 v91, 0x402aaaab, v91
	v_add_f32_e32 v91, 0x40aaab7c, v91
	v_cvt_u32_f32_e32 v91, v91
	v_min_u32_e32 v91, 31, v91
	v_cndmask_b32_e32 v91, v91, v90, vcc
	v_lshl_add_u32 v92, v91, 6, s42
	ds_read_b32 v105, v92
	v_lshl_add_u32 v106, v104, 2, s14
	v_mov_b32_e32 v100, 0xf149f2ca
	v_mov_b32_e32 v101, 0xf149f2ca
	v_mov_b32_e32 v102, 0xf149f2ca
	v_mov_b32_e32 v103, 0xf149f2ca
	v_lshl_add_u32 v93, v88, 4, s13
	ds_write_b128 v93, v[100:103]
	v_add_u32_e32 v94, 0x80, v88
	v_min_u32_e32 v94, 0xdf, v94
	v_lshl_add_u32 v93, v94, 4, s13
	ds_write_b128 v93, v[100:103]
	v_min_u32_e32 v94, 0x21, v88
	v_lshl_add_u32 v93, v94, 4, s15
	ds_write_b128 v93, v[100:103]
	s_waitcnt lgkmcnt(0)
	ds_write_b32 v106, v105
	s_movk_i32 s42, 0x39d

.LBB0_1037:
	s_lshl_b32 s16, s7, 6
	s_add_i32 s29, s16, s28
	v_or_b32_e32 v134, s29, v123
	s_ashr_i32 s7, s6, 31
	s_lshl_b32 s12, s6, 8
	v_ashrrev_i32_e32 v135, 31, v134
	s_lshl_b32 s8, s6, 6
	s_lshl_b64 s[10:11], s[6:7], 21
	s_ashr_i32 s13, s12, 31
	s_lshl_b32 s6, s6, 2
	v_lshlrev_b64 v[2:3], 13, v[134:135]
	s_ashr_i32 s9, s8, 31
	s_ashr_i32 s7, s6, 31
	v_lshl_add_u64 v[2:3], s[80:81], 0, v[2:3]
	s_lshl_b64 s[12:13], s[12:13], 1
	v_lshl_add_u64 v[4:5], v[2:3], 0, s[12:13]
	s_lshl_b64 s[14:15], s[6:7], 1
	s_lshl_b64 s[8:9], s[8:9], 1
	v_lshl_add_u64 v[4:5], v[4:5], 0, v[0:1]
	v_mov_b32_e32 v129, v1
	v_or_b32_e32 v132, 4, v134
	s_add_u32 s8, s94, s8
	v_lshl_add_u64 v[4:5], v[4:5], 0, v[128:129]
	v_ashrrev_i32_e32 v133, 31, v132
	s_addc_u32 s9, s95, s9
	s_add_i32 s7, s16, 0xfffffe00
	global_load_dwordx4 v[42:45], v[4:5], off offset:3584
	global_load_dwordx4 v[46:49], v[4:5], off offset:3648
	v_lshl_add_u64 v[2:3], v[2:3], 0, s[14:15]
	v_mov_b32_e32 v131, v1
	v_lshlrev_b64 v[4:5], 13, v[132:133]
	s_add_u32 s10, s82, s10
	v_lshl_add_u64 v[2:3], v[2:3], 0, v[130:131]
	v_lshl_add_u64 v[4:5], s[80:81], 0, v[4:5]
	s_addc_u32 s11, s83, s11
	v_add_co_u32_e32 v2, vcc, s97, v2
	v_lshl_add_u64 v[6:7], v[4:5], 0, s[12:13]
	s_add_u32 s10, s10, 0x400000
	v_addc_co_u32_e32 v3, vcc, 0, v3, vcc
	v_lshl_add_u64 v[6:7], v[6:7], 0, v[0:1]
	s_addc_u32 s11, s11, 0
	s_max_i32 s42, s7, 0
	v_lshl_add_u64 v[6:7], v[6:7], 0, v[128:129]
	global_load_ushort v156, v[2:3], off offset:2080
	global_load_dwordx4 v[34:37], v[6:7], off offset:3584
	v_lshl_add_u64 v[2:3], v[4:5], 0, s[14:15]
	s_lshl_b64 s[12:13], s[42:43], 13
	v_lshl_add_u64 v[2:3], v[2:3], 0, v[130:131]
	s_add_u32 s12, s8, s12
	v_add_co_u32_e32 v2, vcc, s97, v2
	s_addc_u32 s13, s9, s13
	s_lshl_b32 s14, s42, 1
	v_addc_co_u32_e32 v3, vcc, 0, v3, vcc
	s_add_u32 s14, s10, s14
	global_load_dwordx4 v[38:41], v[6:7], off offset:3648
	global_load_ushort v129, v[2:3], off offset:2080
	s_addc_u32 s15, s11, 0
	v_lshl_add_u64 v[2:3], v[124:125], 1, s[12:13]
	s_barrier
	v_lshl_add_u64 v[4:5], v[126:127], 1, s[14:15]
	global_load_dwordx4 v[54:57], v[2:3], off
	global_load_dwordx4 v[50:53], v[4:5], off
	s_add_i32 s42, s7, 64
	s_max_i32 s42, s42, 0
	s_lshl_b64 s[12:13], s[42:43], 13
	s_lshl_b32 s42, s42, 1
	v_lshl_add_u64 v[200:201], v[124:125], 1, s[8:9]
	v_lshl_add_u64 v[202:203], v[126:127], 1, s[10:11]
	v_lshl_add_u64 v[200:201], v[200:201], 0, s[12:13]
	v_lshl_add_u64 v[202:203], v[202:203], 0, s[42:43]
	global_load_dwordx4 v[204:207], v[200:201], off
	s_nop 0
	global_load_dwordx4 v[200:203], v[202:203], off
	s_and_saveexec_b64 s[12:13], s[0:1]
	s_cbranch_execz .LBB0_1044
	v_readfirstlane_b32 s14, v178
	s_lshr_b32 s14, s14, 7
	v_and_b32_e32 v88, 0x7f, v178
	s_mul_i32 s15, s14, 0x1220
	s_add_i32 s15, s15, 0x20000
	s_add_i32 s36, s6, s14
	s_lshl_b32 s36, s36, 2
	s_add_i32 s36, s36, 0x25500
	s_add_i32 s16, s15, 0x800
	s_add_i32 s17, s15, 0x1000
	v_mov_b32_e32 v104, v88
	v_sub_u32_e32 v90, 0x1ff, v104
	v_cvt_f32_u32_e32 v91, v90
	v_log_f32_e32 v91, v91
	v_cmp_gt_u32_e32 vcc, 16, v90
	v_mul_f32_e32 v91, 0x402aaaab, v91
	v_add_f32_e32 v91, 0x40aaab7c, v91
	v_cvt_u32_f32_e32 v91, v91
	v_min_u32_e32 v91, 31, v91
	v_cndmask_b32_e32 v91, v91, v90, vcc
	v_lshl_add_u32 v92, v91, 6, s36
	ds_read_b32 v108, v92
	v_lshl_add_u32 v112, v104, 2, s16
	v_add_u32_e32 v105, 0x80, v88
	v_sub_u32_e32 v90, 0x1ff, v105
	v_cvt_f32_u32_e32 v91, v90
	v_log_f32_e32 v91, v91
	v_cmp_gt_u32_e32 vcc, 16, v90
	v_mul_f32_e32 v91, 0x402aaaab, v91
	v_add_f32_e32 v91, 0x40aaab7c, v91
	v_cvt_u32_f32_e32 v91, v91
	v_min_u32_e32 v91, 31, v91
	v_cndmask_b32_e32 v91, v91, v90, vcc
	v_lshl_add_u32 v92, v91, 6, s36
	ds_read_b32 v109, v92
	v_lshl_add_u32 v113, v105, 2, s16
	v_add_u32_e32 v106, 0x100, v88
	v_sub_u32_e32 v90, 0x1ff, v106
	v_cvt_f32_u32_e32 v91, v90
	v_log_f32_e32 v91, v91
	v_cmp_gt_u32_e32 vcc, 16, v90
	v_mul_f32_e32 v91, 0x402aaaab, v91
	v_add_f32_e32 v91, 0x40aaab7c, v91
	v_cvt_u32_f32_e32 v91, v91
	v_min_u32_e32 v91, 31, v91
	v_cndmask_b32_e32 v91, v91, v90, vcc
	v_lshl_add_u32 v92, v91, 6, s36
	ds_read_b32 v110, v92
	v_lshl_add_u32 v114, v106, 2, s16
	v_add_u32_e32 v107, 0x180, v88
	v_sub_u32_e32 v90, 0x1ff, v107
	v_cvt_f32_u32_e32 v91, v90
	v_log_f32_e32 v91, v91
	v_cmp_gt_u32_e32 vcc, 16, v90
	v_mul_f32_e32 v91, 0x402aaaab, v91
	v_add_f32_e32 v91, 0x40aaab7c, v91
	v_cvt_u32_f32_e32 v91, v91
	v_min_u32_e32 v91, 31, v91
	v_cndmask_b32_e32 v91, v91, v90, vcc
	v_lshl_add_u32 v92, v91, 6, s36
	ds_read_b32 v111, v92
	v_lshl_add_u32 v115, v107, 2, s16
	v_mov_b32_e32 v100, 0xf149f2ca
	v_mov_b32_e32 v101, 0xf149f2ca
	v_mov_b32_e32 v102, 0xf149f2ca
	v_mov_b32_e32 v103, 0xf149f2ca
	v_lshl_add_u32 v93, v88, 4, s15
	ds_write_b128 v93, v[100:103]
	v_min_u32_e32 v94, 0x21, v88
	v_lshl_add_u32 v93, v94, 4, s17
	ds_write_b128 v93, v[100:103]
	s_waitcnt lgkmcnt(0)
	ds_write_b32 v112, v108
	ds_write_b32 v113, v109
	ds_write_b32 v114, v110
	ds_write_b32 v115, v111
	s_lshl_b32 s14, s6, 2
	s_add_i32 s36, s14, 0x25500
	s_movk_i32 s37, 0x22a

.LBB0_1142:
	s_and_saveexec_b64 s[2:3], s[10:11]
	s_cbranch_execz .LBB0_1149
	v_readfirstlane_b32 s4, v154
	s_lshr_b32 s4, s4, 7
	v_and_b32_e32 v108, 0x7f, v154
	s_mul_i32 s5, s4, 0x1220
	s_add_i32 s5, s5, 0x20000
	s_lshl_b32 s14, s4, 2
	s_add_i32 s14, s14, s54
	s_add_i32 s15, s5, 0x3a0
	s_add_i32 s16, s5, 0x1000
	v_mov_b32_e32 v109, s14
	ds_read_b32 v109, v109 offset:1984
	v_mov_b32_e32 v124, v108
	v_sub_u32_e32 v110, 0x317, v124
	v_cvt_f32_u32_e32 v111, v110
	v_log_f32_e32 v111, v111
	v_cmp_gt_u32_e32 vcc, 16, v110
	v_mul_f32_e32 v111, 0x402aaaab, v111
	v_add_f32_e32 v111, 0x40aaab7c, v111
	v_cvt_u32_f32_e32 v111, v111
	v_min_u32_e32 v111, 31, v111
	v_cndmask_b32_e32 v111, v111, v110, vcc
	v_lshl_add_u32 v112, v111, 6, s14
	ds_read_b32 v131, v112
	v_lshl_add_u32 v138, v124, 2, s15
	v_add_u32_e32 v125, 0x80, v108
	v_sub_u32_e32 v110, 0x317, v125
	v_cvt_f32_u32_e32 v111, v110
	v_log_f32_e32 v111, v111
	v_cmp_gt_u32_e32 vcc, 16, v110
	v_mul_f32_e32 v111, 0x402aaaab, v111
	v_add_f32_e32 v111, 0x40aaab7c, v111
	v_cvt_u32_f32_e32 v111, v111
	v_min_u32_e32 v111, 31, v111
	v_cndmask_b32_e32 v111, v111, v110, vcc
	v_lshl_add_u32 v112, v111, 6, s14
	ds_read_b32 v132, v112
	v_lshl_add_u32 v139, v125, 2, s15
	v_add_u32_e32 v126, 0x100, v108
	v_sub_u32_e32 v110, 0x317, v126
	v_cvt_f32_u32_e32 v111, v110
	v_log_f32_e32 v111, v111
	v_cmp_gt_u32_e32 vcc, 16, v110
	v_mul_f32_e32 v111, 0x402aaaab, v111
	v_add_f32_e32 v111, 0x40aaab7c, v111
	v_cvt_u32_f32_e32 v111, v111
	v_min_u32_e32 v111, 31, v111
	v_cndmask_b32_e32 v111, v111, v110, vcc
	v_lshl_add_u32 v112, v111, 6, s14
	ds_read_b32 v133, v112
	v_lshl_add_u32 v140, v126, 2, s15
	v_add_u32_e32 v127, 0x180, v108
	v_sub_u32_e32 v110, 0x317, v127
	v_cvt_f32_u32_e32 v111, v110
	v_log_f32_e32 v111, v111
	v_cmp_gt_u32_e32 vcc, 16, v110
	v_mul_f32_e32 v111, 0x402aaaab, v111
	v_add_f32_e32 v111, 0x40aaab7c, v111
	v_cvt_u32_f32_e32 v111, v111
	v_min_u32_e32 v111, 31, v111
	v_cndmask_b32_e32 v111, v111, v110, vcc
	v_lshl_add_u32 v112, v111, 6, s14
	ds_read_b32 v134, v112
	v_lshl_add_u32 v141, v127, 2, s15
	v_add_u32_e32 v128, 0x200, v108
	v_sub_u32_e32 v110, 0x317, v128
	v_cvt_f32_u32_e32 v111, v110
	v_log_f32_e32 v111, v111
	v_cmp_gt_u32_e32 vcc, 16, v110
	v_mul_f32_e32 v111, 0x402aaaab, v111
	v_add_f32_e32 v111, 0x40aaab7c, v111
	v_cvt_u32_f32_e32 v111, v111
	v_min_u32_e32 v111, 31, v111
	v_cndmask_b32_e32 v111, v111, v110, vcc
	v_lshl_add_u32 v112, v111, 6, s14
	ds_read_b32 v135, v112
	v_lshl_add_u32 v142, v128, 2, s15
	v_add_u32_e32 v129, 0x280, v108
	v_sub_u32_e32 v110, 0x317, v129
	v_cvt_f32_u32_e32 v111, v110
	v_log_f32_e32 v111, v111
	v_cmp_gt_u32_e32 vcc, 16, v110
	v_mul_f32_e32 v111, 0x402aaaab, v111
	v_add_f32_e32 v111, 0x40aaab7c, v111
	v_cvt_u32_f32_e32 v111, v111
	v_min_u32_e32 v111, 31, v111
	v_cndmask_b32_e32 v111, v111, v110, vcc
	v_lshl_add_u32 v112, v111, 6, s14
	ds_read_b32 v136, v112
	v_lshl_add_u32 v143, v129, 2, s15
	v_add_u32_e32 v130, 0x300, v108
	v_min_u32_e32 v130, 0x317, v130
	v_sub_u32_e32 v110, 0x317, v130
	v_cvt_f32_u32_e32 v111, v110
	v_log_f32_e32 v111, v111
	v_cmp_gt_u32_e32 vcc, 16, v110
	v_mul_f32_e32 v111, 0x402aaaab, v111
	v_add_f32_e32 v111, 0x40aaab7c, v111
	v_cvt_u32_f32_e32 v111, v111
	v_min_u32_e32 v111, 31, v111
	v_cndmask_b32_e32 v111, v111, v110, vcc
	v_lshl_add_u32 v112, v111, 6, s14
	ds_read_b32 v137, v112
	v_lshl_add_u32 v144, v130, 2, s15
	v_mov_b32_e32 v120, 0xf149f2ca
	v_mov_b32_e32 v121, 0xf149f2ca
	v_mov_b32_e32 v122, 0xf149f2ca
	v_mov_b32_e32 v123, 0xf149f2ca
	s_waitcnt lgkmcnt(7)
	v_mov_b32_e32 v116, v109
	v_mov_b32_e32 v117, v109
	v_mov_b32_e32 v118, v109
	v_mov_b32_e32 v119, v109
	v_min_u32_e32 v114, 0x39, v108
	v_lshl_add_u32 v113, v114, 4, s5
	ds_write_b128 v113, v[116:119]
	v_min_u32_e32 v114, 0x21, v108
	v_lshl_add_u32 v113, v114, 4, s16
	ds_write_b128 v113, v[120:123]
	s_waitcnt lgkmcnt(0)
	ds_write_b32 v138, v131
	ds_write_b32 v139, v132
	ds_write_b32 v140, v133
	ds_write_b32 v141, v134
	ds_write_b32 v142, v135
	ds_write_b32 v143, v136
	ds_write_b32 v144, v137
	s_movk_i32 s42, 0x260
